# APROJ stage_scales: all unit row-statistic loads issued before one wait (was load-wait-compute per unit)
# speedup vs baseline: 1.0018x; 1.0018x over previous
;     __host__ __device__ bool next(int i, Unit& u) const {
;         const long L = (long)i * G + c; if (L >= nwg) return false;
;         int wgid = (int)L; { const int q = nwg / NXCD, r = nwg % NXCD, xcd = wgid % NXCD, off = wgid / NXCD; wgid = (xcd < r ? xcd * (q + 1) : r * (q + 1) + (xcd - r) * q) + off; }
;         const int nig = WGM * nN, gid = wgid / nig, fm = gid * WGM, gsz = (nM - fm) < WGM ? (nM - fm) : WGM;
;         u.pm = fm + ((wgid % nig) % gsz); u.pn = (wgid % nig) / gsz; u.idx = i; return true;
; template <class Sched> __device__ __forceinline__ void stage_scales(PG8_LAS unsigned char* lds, const Sched& S, const float* rs, bool cols, int ldil, int tid) {
;     ...
;     if (tid < 256) { const int lper = 8 - ldil, c = tid, tm = ((c & ((1 << lper) - 1)) << ldil) + (c >> lper);
;         float eps = 1e-6f; asm volatile("" : "+s"(eps));
;         for (int i = 0; i < 16 && S.next(i, u); ++i) { const f32x4 a = *(const f32x4*)(rs + 4 * (size_t)(cols ? u.pn * BM + tm : u.pm * BM + tid));
;             tab[i * 256 + tid] = __builtin_amdgcn_rsqf(((a[0] + a[1]) + (a[2] + a[3])) * (1.0f / 1024.0f) + eps); } }
.LBB0_269:
	s_and_b64 vcc, exec, s[2:3]
	s_cbranch_vccz .LBB0_305
	v_readlane_b32 s18, v254, 59
	s_cmp_gt_i32 s18, 1
	s_cbranch_scc0 .LBB0_306
	s_mov_b64 s[20:21], s[16:17]
	s_cmp_gt_i32 s18, 3
	s_mov_b64 s[2:3], -1
	s_movk_i32 s17, 0xc1
	s_cbranch_scc0 .LBB0_309
	v_mbcnt_lo_u32_b32 v2, -1, 0
	v_mbcnt_hi_u32_b32 v2, -1, v2
	s_movk_i32 s0, 0x100
	v_add_u32_e32 v1, s30, v2
	v_cmp_gt_i32_e32 vcc, s0, v1
	s_and_saveexec_b64 s[2:3], vcc
	s_cbranch_execz .LBB0_290
	s_mov_b32 s6, 0x358637bd
	s_cmpk_gt_i32 s90, 0x5ff
	s_cbranch_scc1 .LBB0_290
	s_ashr_i32 s0, s90, 31
	s_lshr_b32 s1, s0, 29
	s_add_i32 s1, s90, s1
	s_ashr_i32 s4, s1, 3
	s_and_b32 s1, s1, -8
	s_ashr_i32 s7, s88, 31
	s_sub_i32 s1, s90, s1
	s_cmp_lt_i32 s1, 0
	s_cselect_b32 s5, s17, 0xc0
	s_mul_i32 s1, s1, s5
	s_add_i32 s1, s1, s4
	s_mul_hi_i32 s4, s1, 0x2aaaaaab
	s_lshr_b32 s5, s4, 31
	s_ashr_i32 s4, s4, 4
	s_add_i32 s4, s4, s5
	s_mul_i32 s5, s4, 0x60
	s_lshl_b32 s4, s4, 3
	s_sub_i32 s1, s1, s5
	s_sub_i32 s5, 0x80, s4
	s_min_i32 s5, s5, 8
	s_abs_i32 s5, s5
	v_cvt_f32_u32_e32 v4, s5
	s_sub_i32 s9, 0, s5
	s_ashr_i32 s8, s1, 31
	s_abs_i32 s1, s1
	v_rcp_iflag_f32_e32 v4, v4
	v_lshl_add_u32 v0, v1, 2, 0
	v_add_u32_e32 v0, 0x20000, v0
	v_mul_f32_e32 v4, 0x4f7ffffe, v4
	v_cvt_u32_f32_e32 v4, v4
	s_nop 0
	v_readfirstlane_b32 s10, v4
	s_mul_i32 s9, s9, s10
	s_mul_hi_u32 s9, s10, s9
	s_add_i32 s10, s10, s9
	s_mul_hi_u32 s9, s1, s10
	s_mul_i32 s9, s9, s5
	s_sub_i32 s1, s1, s9
	s_sub_i32 s9, s1, s5
	s_cmp_ge_u32 s1, s5
	s_cselect_b32 s1, s9, s1
	s_sub_i32 s9, s1, s5
	s_cmp_ge_u32 s1, s5
	s_cselect_b32 s1, s9, s1
	s_xor_b32 s1, s1, s8
	s_sub_i32 s1, s1, s8
	s_add_i32 s4, s4, s1
	v_lshl_add_u32 v4, s4, 8, v1
	v_readlane_b32 s4, v254, 63
	v_ashrrev_i32_e32 v5, 31, v4
	v_readlane_b32 s5, v255, 0
	s_nop 1
	v_lshl_add_u64 v[4:5], v[4:5], 4, s[4:5]
	global_load_dwordx4 v[64:67], v[4:5], off
	s_add_u32 s4, s88, s90
	s_addc_u32 s5, s7, s0
	v_cmp_gt_i64_e32 vcc, s[4:5], v[252:253]
	s_and_b64 vcc, exec, vcc
	s_cbranch_vccnz .LBB0_290
	s_ashr_i32 s0, s4, 31
	s_lshr_b32 s0, s0, 29
	s_add_i32 s0, s4, s0
	s_ashr_i32 s1, s0, 3
	s_and_b32 s0, s0, -8
	s_sub_i32 s0, s4, s0
	s_cmp_lt_i32 s0, 0
	s_cselect_b32 s8, s17, 0xc0
	s_mul_i32 s0, s0, s8
	s_add_i32 s0, s0, s1
	s_mul_hi_i32 s1, s0, 0x2aaaaaab
	s_lshr_b32 s8, s1, 31
	s_ashr_i32 s1, s1, 4
	s_add_i32 s1, s1, s8
	s_mul_i32 s8, s1, 0x60
	s_lshl_b32 s1, s1, 3
	s_sub_i32 s0, s0, s8
	s_sub_i32 s8, 0x80, s1
	s_min_i32 s8, s8, 8
	s_abs_i32 s8, s8
	v_cvt_f32_u32_e32 v4, s8
	s_sub_i32 s10, 0, s8
	s_ashr_i32 s9, s0, 31
	s_abs_i32 s0, s0
	v_rcp_iflag_f32_e32 v4, v4
	s_nop 0
	v_mul_f32_e32 v4, 0x4f7ffffe, v4
	v_cvt_u32_f32_e32 v4, v4
	s_nop 0
	v_readfirstlane_b32 s11, v4
	s_mul_i32 s10, s10, s11
	s_mul_hi_u32 s10, s11, s10
	s_add_i32 s11, s11, s10
	s_mul_hi_u32 s10, s0, s11
	s_mul_i32 s10, s10, s8
	s_sub_i32 s0, s0, s10
	s_sub_i32 s10, s0, s8
	s_cmp_ge_u32 s0, s8
	s_cselect_b32 s0, s10, s0
	s_sub_i32 s10, s0, s8
	s_cmp_ge_u32 s0, s8
	s_cselect_b32 s0, s10, s0
	s_xor_b32 s0, s0, s9
	s_sub_i32 s0, s0, s9
	s_add_i32 s1, s1, s0
	v_lshl_add_u32 v4, s1, 8, v1
	v_readlane_b32 s0, v254, 63
	v_ashrrev_i32_e32 v5, 31, v4
	v_readlane_b32 s1, v255, 0
	s_add_u32 s4, s4, s88
	s_addc_u32 s5, s5, s7
	v_lshl_add_u64 v[4:5], v[4:5], 4, s[0:1]
	global_load_dwordx4 v[68:71], v[4:5], off
	v_cmp_gt_i64_e32 vcc, s[4:5], v[252:253]
	s_and_b64 vcc, exec, vcc
	s_cbranch_vccnz .LBB0_290
	s_ashr_i32 s0, s4, 31
	s_lshr_b32 s0, s0, 29
	s_add_i32 s0, s4, s0
	s_ashr_i32 s1, s0, 3
	s_and_b32 s0, s0, -8
	s_sub_i32 s0, s4, s0
	s_cmp_lt_i32 s0, 0
	s_cselect_b32 s8, s17, 0xc0
	s_mul_i32 s0, s0, s8
	s_add_i32 s0, s0, s1
	s_mul_hi_i32 s1, s0, 0x2aaaaaab
	s_lshr_b32 s8, s1, 31
	s_ashr_i32 s1, s1, 4
	s_add_i32 s1, s1, s8
	s_mul_i32 s8, s1, 0x60
	s_lshl_b32 s1, s1, 3
	s_sub_i32 s0, s0, s8
	s_sub_i32 s8, 0x80, s1
	s_min_i32 s8, s8, 8
	s_abs_i32 s8, s8
	v_cvt_f32_u32_e32 v4, s8
	s_sub_i32 s10, 0, s8
	s_ashr_i32 s9, s0, 31
	s_abs_i32 s0, s0
	v_rcp_iflag_f32_e32 v4, v4
	s_nop 0
	v_mul_f32_e32 v4, 0x4f7ffffe, v4
	v_cvt_u32_f32_e32 v4, v4
	s_nop 0
	v_readfirstlane_b32 s11, v4
	s_mul_i32 s10, s10, s11
	s_mul_hi_u32 s10, s11, s10
	s_add_i32 s11, s11, s10
	s_mul_hi_u32 s10, s0, s11
	s_mul_i32 s10, s10, s8
	s_sub_i32 s0, s0, s10
	s_sub_i32 s10, s0, s8
	s_cmp_ge_u32 s0, s8
	s_cselect_b32 s0, s10, s0
	s_sub_i32 s10, s0, s8
	s_cmp_ge_u32 s0, s8
	s_cselect_b32 s0, s10, s0
	s_xor_b32 s0, s0, s9
	s_sub_i32 s0, s0, s9
	s_add_i32 s1, s1, s0
	v_lshl_add_u32 v4, s1, 8, v1
	v_readlane_b32 s0, v254, 63
	v_ashrrev_i32_e32 v5, 31, v4
	v_readlane_b32 s1, v255, 0
	s_add_u32 s4, s4, s88
	s_addc_u32 s5, s5, s7
	v_lshl_add_u64 v[4:5], v[4:5], 4, s[0:1]
	global_load_dwordx4 v[72:75], v[4:5], off
	v_cmp_gt_i64_e32 vcc, s[4:5], v[252:253]
	s_and_b64 vcc, exec, vcc
	s_cbranch_vccnz .LBB0_290
	s_ashr_i32 s0, s4, 31
	s_lshr_b32 s0, s0, 29
	s_add_i32 s0, s4, s0
	s_ashr_i32 s1, s0, 3
	s_and_b32 s0, s0, -8
	s_sub_i32 s0, s4, s0
	s_cmp_lt_i32 s0, 0
	s_cselect_b32 s8, s17, 0xc0
	s_mul_i32 s0, s0, s8
	s_add_i32 s0, s0, s1
	s_mul_hi_i32 s1, s0, 0x2aaaaaab
	s_lshr_b32 s8, s1, 31
	s_ashr_i32 s1, s1, 4
	s_add_i32 s1, s1, s8
	s_mul_i32 s8, s1, 0x60
	s_lshl_b32 s1, s1, 3
	s_sub_i32 s0, s0, s8
	s_sub_i32 s8, 0x80, s1
	s_min_i32 s8, s8, 8
	s_abs_i32 s8, s8
	v_cvt_f32_u32_e32 v4, s8
	s_sub_i32 s10, 0, s8
	s_ashr_i32 s9, s0, 31
	s_abs_i32 s0, s0
	v_rcp_iflag_f32_e32 v4, v4
	s_nop 0
	v_mul_f32_e32 v4, 0x4f7ffffe, v4
	v_cvt_u32_f32_e32 v4, v4
	s_nop 0
	v_readfirstlane_b32 s11, v4
	s_mul_i32 s10, s10, s11
	s_mul_hi_u32 s10, s11, s10
	s_add_i32 s11, s11, s10
	s_mul_hi_u32 s10, s0, s11
	s_mul_i32 s10, s10, s8
	s_sub_i32 s0, s0, s10
	s_sub_i32 s10, s0, s8
	s_cmp_ge_u32 s0, s8
	s_cselect_b32 s0, s10, s0
	s_sub_i32 s10, s0, s8
	s_cmp_ge_u32 s0, s8
	s_cselect_b32 s0, s10, s0
	s_xor_b32 s0, s0, s9
	s_sub_i32 s0, s0, s9
	s_add_i32 s1, s1, s0
	v_lshl_add_u32 v4, s1, 8, v1
	v_readlane_b32 s0, v254, 63
	v_ashrrev_i32_e32 v5, 31, v4
	v_readlane_b32 s1, v255, 0
	s_add_u32 s4, s4, s88
	s_addc_u32 s5, s5, s7
	v_lshl_add_u64 v[4:5], v[4:5], 4, s[0:1]
	global_load_dwordx4 v[76:79], v[4:5], off
	v_cmp_gt_i64_e32 vcc, s[4:5], v[252:253]
	s_and_b64 vcc, exec, vcc
	s_cbranch_vccnz .LBB0_290
;     __host__ __device__ bool next(int i, Unit& u) const {
;         const long L = (long)i * G + c; if (L >= nwg) return false;
;         int wgid = (int)L; { const int q = nwg / NXCD, r = nwg % NXCD, xcd = wgid % NXCD, off = wgid / NXCD; wgid = (xcd < r ? xcd * (q + 1) : r * (q + 1) + (xcd - r) * q) + off; }
;         const int nig = WGM * nN, gid = wgid / nig, fm = gid * WGM, gsz = (nM - fm) < WGM ? (nM - fm) : WGM;
;         u.pm = fm + ((wgid % nig) % gsz); u.pn = (wgid % nig) / gsz; u.idx = i; return true;
; template <class Sched> __device__ __forceinline__ void stage_scales(PG8_LAS unsigned char* lds, const Sched& S, const float* rs, bool cols, int ldil, int tid) {
;     ...
;     if (tid < 256) { const int lper = 8 - ldil, c = tid, tm = ((c & ((1 << lper) - 1)) << ldil) + (c >> lper);
;         float eps = 1e-6f; asm volatile("" : "+s"(eps));
;         for (int i = 0; i < 16 && S.next(i, u); ++i) { const f32x4 a = *(const f32x4*)(rs + 4 * (size_t)(cols ? u.pn * BM + tm : u.pm * BM + tid));
;             tab[i * 256 + tid] = __builtin_amdgcn_rsqf(((a[0] + a[1]) + (a[2] + a[3])) * (1.0f / 1024.0f) + eps); } }
	s_ashr_i32 s0, s4, 31
	s_lshr_b32 s0, s0, 29
	s_add_i32 s0, s4, s0
	s_ashr_i32 s1, s0, 3
	s_and_b32 s0, s0, -8
	s_sub_i32 s0, s4, s0
	s_cmp_lt_i32 s0, 0
	s_cselect_b32 s8, s17, 0xc0
	s_mul_i32 s0, s0, s8
	s_add_i32 s0, s0, s1
	s_mul_hi_i32 s1, s0, 0x2aaaaaab
	s_lshr_b32 s8, s1, 31
	s_ashr_i32 s1, s1, 4
	s_add_i32 s1, s1, s8
	s_mul_i32 s8, s1, 0x60
	s_lshl_b32 s1, s1, 3
	s_sub_i32 s0, s0, s8
	s_sub_i32 s8, 0x80, s1
	s_min_i32 s8, s8, 8
	s_abs_i32 s8, s8
	v_cvt_f32_u32_e32 v4, s8
	s_sub_i32 s10, 0, s8
	s_ashr_i32 s9, s0, 31
	s_abs_i32 s0, s0
	v_rcp_iflag_f32_e32 v4, v4
	s_nop 0
	v_mul_f32_e32 v4, 0x4f7ffffe, v4
	v_cvt_u32_f32_e32 v4, v4
	s_nop 0
	v_readfirstlane_b32 s11, v4
	s_mul_i32 s10, s10, s11
	s_mul_hi_u32 s10, s11, s10
	s_add_i32 s11, s11, s10
	s_mul_hi_u32 s10, s0, s11
	s_mul_i32 s10, s10, s8
	s_sub_i32 s0, s0, s10
	s_sub_i32 s10, s0, s8
	s_cmp_ge_u32 s0, s8
	s_cselect_b32 s0, s10, s0
	s_sub_i32 s10, s0, s8
	s_cmp_ge_u32 s0, s8
	s_cselect_b32 s0, s10, s0
	s_xor_b32 s0, s0, s9
	s_sub_i32 s0, s0, s9
	s_add_i32 s1, s1, s0
	v_lshl_add_u32 v4, s1, 8, v1
	v_readlane_b32 s0, v254, 63
	v_ashrrev_i32_e32 v5, 31, v4
	v_readlane_b32 s1, v255, 0
	s_add_u32 s4, s4, s88
	s_addc_u32 s5, s5, s7
	v_lshl_add_u64 v[4:5], v[4:5], 4, s[0:1]
	global_load_dwordx4 v[80:83], v[4:5], off
	v_cmp_gt_i64_e32 vcc, s[4:5], v[252:253]
	s_and_b64 vcc, exec, vcc
	s_cbranch_vccnz .LBB0_290
	s_ashr_i32 s0, s4, 31
	s_lshr_b32 s0, s0, 29
	s_add_i32 s0, s4, s0
	s_ashr_i32 s1, s0, 3
	s_and_b32 s0, s0, -8
	s_sub_i32 s0, s4, s0
	s_cmp_lt_i32 s0, 0
	s_cselect_b32 s8, s17, 0xc0
	s_mul_i32 s0, s0, s8
	s_add_i32 s0, s0, s1
	s_mul_hi_i32 s1, s0, 0x2aaaaaab
	s_lshr_b32 s8, s1, 31
	s_ashr_i32 s1, s1, 4
	s_add_i32 s1, s1, s8
	s_mul_i32 s8, s1, 0x60
	s_lshl_b32 s1, s1, 3
	s_sub_i32 s0, s0, s8
	s_sub_i32 s8, 0x80, s1
	s_min_i32 s8, s8, 8
	s_abs_i32 s8, s8
	v_cvt_f32_u32_e32 v4, s8
	s_sub_i32 s10, 0, s8
	s_ashr_i32 s9, s0, 31
	s_abs_i32 s0, s0
	v_rcp_iflag_f32_e32 v4, v4
	s_nop 0
	v_mul_f32_e32 v4, 0x4f7ffffe, v4
	v_cvt_u32_f32_e32 v4, v4
	s_nop 0
	v_readfirstlane_b32 s11, v4
	s_mul_i32 s10, s10, s11
	s_mul_hi_u32 s10, s11, s10
	s_add_i32 s11, s11, s10
	s_mul_hi_u32 s10, s0, s11
	s_mul_i32 s10, s10, s8
	s_sub_i32 s0, s0, s10
	s_sub_i32 s10, s0, s8
	s_cmp_ge_u32 s0, s8
	s_cselect_b32 s0, s10, s0
	s_sub_i32 s10, s0, s8
	s_cmp_ge_u32 s0, s8
	s_cselect_b32 s0, s10, s0
	s_xor_b32 s0, s0, s9
	s_sub_i32 s0, s0, s9
	s_add_i32 s1, s1, s0
	v_lshl_add_u32 v4, s1, 8, v1
	v_readlane_b32 s0, v254, 63
	v_ashrrev_i32_e32 v5, 31, v4
	v_readlane_b32 s1, v255, 0
	s_add_u32 s4, s4, s88
	s_addc_u32 s5, s5, s7
	v_lshl_add_u64 v[4:5], v[4:5], 4, s[0:1]
	global_load_dwordx4 v[84:87], v[4:5], off
	v_cmp_gt_i64_e32 vcc, s[4:5], v[252:253]
	s_and_b64 vcc, exec, vcc
	s_cbranch_vccnz .LBB0_290
	s_ashr_i32 s0, s4, 31
	s_lshr_b32 s0, s0, 29
	s_add_i32 s0, s4, s0
	s_ashr_i32 s1, s0, 3
	s_and_b32 s0, s0, -8
	s_sub_i32 s0, s4, s0
	s_cmp_lt_i32 s0, 0
	s_cselect_b32 s8, s17, 0xc0
	s_mul_i32 s0, s0, s8
	s_add_i32 s0, s0, s1
	s_mul_hi_i32 s1, s0, 0x2aaaaaab
	s_lshr_b32 s8, s1, 31
	s_ashr_i32 s1, s1, 4
	s_add_i32 s1, s1, s8
	s_mul_i32 s8, s1, 0x60
	s_lshl_b32 s1, s1, 3
	s_sub_i32 s0, s0, s8
	s_sub_i32 s8, 0x80, s1
	s_min_i32 s8, s8, 8
	s_abs_i32 s8, s8
	v_cvt_f32_u32_e32 v4, s8
	s_sub_i32 s10, 0, s8
	s_ashr_i32 s9, s0, 31
	s_abs_i32 s0, s0
	v_rcp_iflag_f32_e32 v4, v4
	s_nop 0
	v_mul_f32_e32 v4, 0x4f7ffffe, v4
	v_cvt_u32_f32_e32 v4, v4
	s_nop 0
	v_readfirstlane_b32 s11, v4
	s_mul_i32 s10, s10, s11
	s_mul_hi_u32 s10, s11, s10
	s_add_i32 s11, s11, s10
	s_mul_hi_u32 s10, s0, s11
	s_mul_i32 s10, s10, s8
	s_sub_i32 s0, s0, s10
	s_sub_i32 s10, s0, s8
	s_cmp_ge_u32 s0, s8
	s_cselect_b32 s0, s10, s0
	s_sub_i32 s10, s0, s8
	s_cmp_ge_u32 s0, s8
	s_cselect_b32 s0, s10, s0
	s_xor_b32 s0, s0, s9
	s_sub_i32 s0, s0, s9
	s_add_i32 s1, s1, s0
	v_lshl_add_u32 v4, s1, 8, v1
	v_readlane_b32 s0, v254, 63
	v_ashrrev_i32_e32 v5, 31, v4
	v_readlane_b32 s1, v255, 0
	s_add_u32 s4, s4, s88
	s_addc_u32 s5, s5, s7
	v_lshl_add_u64 v[4:5], v[4:5], 4, s[0:1]
	global_load_dwordx4 v[88:91], v[4:5], off
	v_cmp_gt_i64_e32 vcc, s[4:5], v[252:253]
	s_and_b64 vcc, exec, vcc
	s_cbranch_vccnz .LBB0_290
	s_ashr_i32 s0, s4, 31
	s_lshr_b32 s0, s0, 29
	s_add_i32 s0, s4, s0
	s_ashr_i32 s1, s0, 3
	s_and_b32 s0, s0, -8
	s_sub_i32 s0, s4, s0
	s_cmp_lt_i32 s0, 0
	s_cselect_b32 s8, s17, 0xc0
	s_mul_i32 s0, s0, s8
	s_add_i32 s0, s0, s1
	s_mul_hi_i32 s1, s0, 0x2aaaaaab
	s_lshr_b32 s8, s1, 31
	s_ashr_i32 s1, s1, 4
	s_add_i32 s1, s1, s8
	s_mul_i32 s8, s1, 0x60
	s_lshl_b32 s1, s1, 3
	s_sub_i32 s0, s0, s8
	s_sub_i32 s8, 0x80, s1
	s_min_i32 s8, s8, 8
	s_abs_i32 s8, s8
	v_cvt_f32_u32_e32 v4, s8
	s_sub_i32 s10, 0, s8
	s_ashr_i32 s9, s0, 31
	s_abs_i32 s0, s0
	v_rcp_iflag_f32_e32 v4, v4
	s_nop 0
	v_mul_f32_e32 v4, 0x4f7ffffe, v4
	v_cvt_u32_f32_e32 v4, v4
	s_nop 0
	v_readfirstlane_b32 s11, v4
	s_mul_i32 s10, s10, s11
	s_mul_hi_u32 s10, s11, s10
	s_add_i32 s11, s11, s10
	s_mul_hi_u32 s10, s0, s11
	s_mul_i32 s10, s10, s8
	s_sub_i32 s0, s0, s10
	s_sub_i32 s10, s0, s8
	s_cmp_ge_u32 s0, s8
	s_cselect_b32 s0, s10, s0
	s_sub_i32 s10, s0, s8
	s_cmp_ge_u32 s0, s8
	s_cselect_b32 s0, s10, s0
	s_xor_b32 s0, s0, s9
	s_sub_i32 s0, s0, s9
	s_add_i32 s1, s1, s0
	v_lshl_add_u32 v4, s1, 8, v1
	v_readlane_b32 s0, v254, 63
	v_ashrrev_i32_e32 v5, 31, v4
	v_readlane_b32 s1, v255, 0
	s_add_u32 s4, s4, s88
	s_addc_u32 s5, s5, s7
	v_lshl_add_u64 v[4:5], v[4:5], 4, s[0:1]
	global_load_dwordx4 v[92:95], v[4:5], off
	v_cmp_gt_i64_e32 vcc, s[4:5], v[252:253]
	s_and_b64 vcc, exec, vcc
	s_cbranch_vccnz .LBB0_290
;     __host__ __device__ bool next(int i, Unit& u) const {
;         const long L = (long)i * G + c; if (L >= nwg) return false;
;         int wgid = (int)L; { const int q = nwg / NXCD, r = nwg % NXCD, xcd = wgid % NXCD, off = wgid / NXCD; wgid = (xcd < r ? xcd * (q + 1) : r * (q + 1) + (xcd - r) * q) + off; }
;         const int nig = WGM * nN, gid = wgid / nig, fm = gid * WGM, gsz = (nM - fm) < WGM ? (nM - fm) : WGM;
;         u.pm = fm + ((wgid % nig) % gsz); u.pn = (wgid % nig) / gsz; u.idx = i; return true;
; template <class Sched> __device__ __forceinline__ void stage_scales(PG8_LAS unsigned char* lds, const Sched& S, const float* rs, bool cols, int ldil, int tid) {
;     ...
;     if (tid < 256) { const int lper = 8 - ldil, c = tid, tm = ((c & ((1 << lper) - 1)) << ldil) + (c >> lper);
;         float eps = 1e-6f; asm volatile("" : "+s"(eps));
;         for (int i = 0; i < 16 && S.next(i, u); ++i) { const f32x4 a = *(const f32x4*)(rs + 4 * (size_t)(cols ? u.pn * BM + tm : u.pm * BM + tid));
;             tab[i * 256 + tid] = __builtin_amdgcn_rsqf(((a[0] + a[1]) + (a[2] + a[3])) * (1.0f / 1024.0f) + eps); } }
	s_ashr_i32 s0, s4, 31
	s_lshr_b32 s0, s0, 29
	s_add_i32 s0, s4, s0
	s_ashr_i32 s1, s0, 3
	s_and_b32 s0, s0, -8
	s_sub_i32 s0, s4, s0
	s_cmp_lt_i32 s0, 0
	s_cselect_b32 s8, s17, 0xc0
	s_mul_i32 s0, s0, s8
	s_add_i32 s0, s0, s1
	s_mul_hi_i32 s1, s0, 0x2aaaaaab
	s_lshr_b32 s8, s1, 31
	s_ashr_i32 s1, s1, 4
	s_add_i32 s1, s1, s8
	s_mul_i32 s8, s1, 0x60
	s_lshl_b32 s1, s1, 3
	s_sub_i32 s0, s0, s8
	s_sub_i32 s8, 0x80, s1
	s_min_i32 s8, s8, 8
	s_abs_i32 s8, s8
	v_cvt_f32_u32_e32 v4, s8
	s_sub_i32 s10, 0, s8
	s_ashr_i32 s9, s0, 31
	s_abs_i32 s0, s0
	v_rcp_iflag_f32_e32 v4, v4
	s_nop 0
	v_mul_f32_e32 v4, 0x4f7ffffe, v4
	v_cvt_u32_f32_e32 v4, v4
	s_nop 0
	v_readfirstlane_b32 s11, v4
	s_mul_i32 s10, s10, s11
	s_mul_hi_u32 s10, s11, s10
	s_add_i32 s11, s11, s10
	s_mul_hi_u32 s10, s0, s11
	s_mul_i32 s10, s10, s8
	s_sub_i32 s0, s0, s10
	s_sub_i32 s10, s0, s8
	s_cmp_ge_u32 s0, s8
	s_cselect_b32 s0, s10, s0
	s_sub_i32 s10, s0, s8
	s_cmp_ge_u32 s0, s8
	s_cselect_b32 s0, s10, s0
	s_xor_b32 s0, s0, s9
	s_sub_i32 s0, s0, s9
	s_add_i32 s1, s1, s0
	v_lshl_add_u32 v4, s1, 8, v1
	v_readlane_b32 s0, v254, 63
	v_ashrrev_i32_e32 v5, 31, v4
	v_readlane_b32 s1, v255, 0
	s_add_u32 s4, s4, s88
	s_addc_u32 s5, s5, s7
	v_lshl_add_u64 v[4:5], v[4:5], 4, s[0:1]
	global_load_dwordx4 v[96:99], v[4:5], off
	v_cmp_gt_i64_e32 vcc, s[4:5], v[252:253]
	s_and_b64 vcc, exec, vcc
	s_cbranch_vccnz .LBB0_290
	s_ashr_i32 s0, s4, 31
	s_lshr_b32 s0, s0, 29
	s_add_i32 s0, s4, s0
	s_ashr_i32 s1, s0, 3
	s_and_b32 s0, s0, -8
	s_sub_i32 s0, s4, s0
	s_cmp_lt_i32 s0, 0
	s_cselect_b32 s8, s17, 0xc0
	s_mul_i32 s0, s0, s8
	s_add_i32 s0, s0, s1
	s_mul_hi_i32 s1, s0, 0x2aaaaaab
	s_lshr_b32 s8, s1, 31
	s_ashr_i32 s1, s1, 4
	s_add_i32 s1, s1, s8
	s_mul_i32 s8, s1, 0x60
	s_lshl_b32 s1, s1, 3
	s_sub_i32 s0, s0, s8
	s_sub_i32 s8, 0x80, s1
	s_min_i32 s8, s8, 8
	s_abs_i32 s8, s8
	v_cvt_f32_u32_e32 v4, s8
	s_sub_i32 s10, 0, s8
	s_ashr_i32 s9, s0, 31
	s_abs_i32 s0, s0
	v_rcp_iflag_f32_e32 v4, v4
	s_nop 0
	v_mul_f32_e32 v4, 0x4f7ffffe, v4
	v_cvt_u32_f32_e32 v4, v4
	s_nop 0
	v_readfirstlane_b32 s11, v4
	s_mul_i32 s10, s10, s11
	s_mul_hi_u32 s10, s11, s10
	s_add_i32 s11, s11, s10
	s_mul_hi_u32 s10, s0, s11
	s_mul_i32 s10, s10, s8
	s_sub_i32 s0, s0, s10
	s_sub_i32 s10, s0, s8
	s_cmp_ge_u32 s0, s8
	s_cselect_b32 s0, s10, s0
	s_sub_i32 s10, s0, s8
	s_cmp_ge_u32 s0, s8
	s_cselect_b32 s0, s10, s0
	s_xor_b32 s0, s0, s9
	s_sub_i32 s0, s0, s9
	s_add_i32 s1, s1, s0
	v_lshl_add_u32 v4, s1, 8, v1
	v_readlane_b32 s0, v254, 63
	v_ashrrev_i32_e32 v5, 31, v4
	v_readlane_b32 s1, v255, 0
	s_add_u32 s4, s4, s88
	s_addc_u32 s5, s5, s7
	v_lshl_add_u64 v[4:5], v[4:5], 4, s[0:1]
	global_load_dwordx4 v[100:103], v[4:5], off
	v_cmp_gt_i64_e32 vcc, s[4:5], v[252:253]
	s_and_b64 vcc, exec, vcc
	s_cbranch_vccnz .LBB0_290
	s_ashr_i32 s0, s4, 31
	s_lshr_b32 s0, s0, 29
	s_add_i32 s0, s4, s0
	s_ashr_i32 s1, s0, 3
	s_and_b32 s0, s0, -8
	s_sub_i32 s0, s4, s0
	s_cmp_lt_i32 s0, 0
	s_cselect_b32 s8, s17, 0xc0
	s_mul_i32 s0, s0, s8
	s_add_i32 s0, s0, s1
	s_mul_hi_i32 s1, s0, 0x2aaaaaab
	s_lshr_b32 s8, s1, 31
	s_ashr_i32 s1, s1, 4
	s_add_i32 s1, s1, s8
	s_mul_i32 s8, s1, 0x60
	s_lshl_b32 s1, s1, 3
	s_sub_i32 s0, s0, s8
	s_sub_i32 s8, 0x80, s1
	s_min_i32 s8, s8, 8
	s_abs_i32 s8, s8
	v_cvt_f32_u32_e32 v4, s8
	s_sub_i32 s10, 0, s8
	s_ashr_i32 s9, s0, 31
	s_abs_i32 s0, s0
	v_rcp_iflag_f32_e32 v4, v4
	s_nop 0
	v_mul_f32_e32 v4, 0x4f7ffffe, v4
	v_cvt_u32_f32_e32 v4, v4
	s_nop 0
	v_readfirstlane_b32 s11, v4
	s_mul_i32 s10, s10, s11
	s_mul_hi_u32 s10, s11, s10
	s_add_i32 s11, s11, s10
	s_mul_hi_u32 s10, s0, s11
	s_mul_i32 s10, s10, s8
	s_sub_i32 s0, s0, s10
	s_sub_i32 s10, s0, s8
	s_cmp_ge_u32 s0, s8
	s_cselect_b32 s0, s10, s0
	s_sub_i32 s10, s0, s8
	s_cmp_ge_u32 s0, s8
	s_cselect_b32 s0, s10, s0
	s_xor_b32 s0, s0, s9
	s_sub_i32 s0, s0, s9
	s_add_i32 s1, s1, s0
	v_lshl_add_u32 v4, s1, 8, v1
	v_readlane_b32 s0, v254, 63
	v_ashrrev_i32_e32 v5, 31, v4
	v_readlane_b32 s1, v255, 0
	s_add_u32 s4, s4, s88
	s_addc_u32 s5, s5, s7
	v_lshl_add_u64 v[4:5], v[4:5], 4, s[0:1]
	global_load_dwordx4 v[104:107], v[4:5], off
	v_cmp_gt_i64_e32 vcc, s[4:5], v[252:253]
	s_and_b64 vcc, exec, vcc
	s_cbranch_vccnz .LBB0_290
	s_ashr_i32 s0, s4, 31
	s_lshr_b32 s0, s0, 29
	s_add_i32 s0, s4, s0
	s_ashr_i32 s1, s0, 3
	s_and_b32 s0, s0, -8
	s_sub_i32 s0, s4, s0
	s_cmp_lt_i32 s0, 0
	s_cselect_b32 s8, s17, 0xc0
	s_mul_i32 s0, s0, s8
	s_add_i32 s0, s0, s1
	s_mul_hi_i32 s1, s0, 0x2aaaaaab
	s_lshr_b32 s8, s1, 31
	s_ashr_i32 s1, s1, 4
	s_add_i32 s1, s1, s8
	s_mul_i32 s8, s1, 0x60
	s_lshl_b32 s1, s1, 3
	s_sub_i32 s0, s0, s8
	s_sub_i32 s8, 0x80, s1
	s_min_i32 s8, s8, 8
	s_abs_i32 s8, s8
	v_cvt_f32_u32_e32 v4, s8
	s_sub_i32 s10, 0, s8
	s_ashr_i32 s9, s0, 31
	s_abs_i32 s0, s0
	v_rcp_iflag_f32_e32 v4, v4
	s_nop 0
	v_mul_f32_e32 v4, 0x4f7ffffe, v4
	v_cvt_u32_f32_e32 v4, v4
	s_nop 0
	v_readfirstlane_b32 s11, v4
	s_mul_i32 s10, s10, s11
	s_mul_hi_u32 s10, s11, s10
	s_add_i32 s11, s11, s10
	s_mul_hi_u32 s10, s0, s11
	s_mul_i32 s10, s10, s8
	s_sub_i32 s0, s0, s10
	s_sub_i32 s10, s0, s8
	s_cmp_ge_u32 s0, s8
	s_cselect_b32 s0, s10, s0
	s_sub_i32 s10, s0, s8
	s_cmp_ge_u32 s0, s8
	s_cselect_b32 s0, s10, s0
	s_xor_b32 s0, s0, s9
	s_sub_i32 s0, s0, s9
	s_add_i32 s1, s1, s0
	v_lshl_add_u32 v4, s1, 8, v1
	v_readlane_b32 s0, v254, 63
	v_ashrrev_i32_e32 v5, 31, v4
	v_readlane_b32 s1, v255, 0
	s_add_u32 s4, s4, s88
	s_addc_u32 s5, s5, s7
	v_lshl_add_u64 v[4:5], v[4:5], 4, s[0:1]
	global_load_dwordx4 v[108:111], v[4:5], off
	v_cmp_gt_i64_e32 vcc, s[4:5], v[252:253]
	s_and_b64 vcc, exec, vcc
	s_cbranch_vccnz .LBB0_290
;     __host__ __device__ bool next(int i, Unit& u) const {
;         const long L = (long)i * G + c; if (L >= nwg) return false;
;         int wgid = (int)L; { const int q = nwg / NXCD, r = nwg % NXCD, xcd = wgid % NXCD, off = wgid / NXCD; wgid = (xcd < r ? xcd * (q + 1) : r * (q + 1) + (xcd - r) * q) + off; }
;         const int nig = WGM * nN, gid = wgid / nig, fm = gid * WGM, gsz = (nM - fm) < WGM ? (nM - fm) : WGM;
;         u.pm = fm + ((wgid % nig) % gsz); u.pn = (wgid % nig) / gsz; u.idx = i; return true;
; template <class Sched> __device__ __forceinline__ void stage_scales(PG8_LAS unsigned char* lds, const Sched& S, const float* rs, bool cols, int ldil, int tid) {
;     ...
;     if (tid < 256) { const int lper = 8 - ldil, c = tid, tm = ((c & ((1 << lper) - 1)) << ldil) + (c >> lper);
;         float eps = 1e-6f; asm volatile("" : "+s"(eps));
;         for (int i = 0; i < 16 && S.next(i, u); ++i) { const f32x4 a = *(const f32x4*)(rs + 4 * (size_t)(cols ? u.pn * BM + tm : u.pm * BM + tid));
;             tab[i * 256 + tid] = __builtin_amdgcn_rsqf(((a[0] + a[1]) + (a[2] + a[3])) * (1.0f / 1024.0f) + eps); } }
	s_ashr_i32 s0, s4, 31
	s_lshr_b32 s0, s0, 29
	s_add_i32 s0, s4, s0
	s_ashr_i32 s1, s0, 3
	s_and_b32 s0, s0, -8
	s_sub_i32 s0, s4, s0
	s_cmp_lt_i32 s0, 0
	s_cselect_b32 s8, s17, 0xc0
	s_mul_i32 s0, s0, s8
	s_add_i32 s0, s0, s1
	s_mul_hi_i32 s1, s0, 0x2aaaaaab
	s_lshr_b32 s8, s1, 31
	s_ashr_i32 s1, s1, 4
	s_add_i32 s1, s1, s8
	s_mul_i32 s8, s1, 0x60
	s_lshl_b32 s1, s1, 3
	s_sub_i32 s0, s0, s8
	s_sub_i32 s8, 0x80, s1
	s_min_i32 s8, s8, 8
	s_abs_i32 s8, s8
	v_cvt_f32_u32_e32 v4, s8
	s_sub_i32 s10, 0, s8
	s_ashr_i32 s9, s0, 31
	s_abs_i32 s0, s0
	v_rcp_iflag_f32_e32 v4, v4
	s_nop 0
	v_mul_f32_e32 v4, 0x4f7ffffe, v4
	v_cvt_u32_f32_e32 v4, v4
	s_nop 0
	v_readfirstlane_b32 s11, v4
	s_mul_i32 s10, s10, s11
	s_mul_hi_u32 s10, s11, s10
	s_add_i32 s11, s11, s10
	s_mul_hi_u32 s10, s0, s11
	s_mul_i32 s10, s10, s8
	s_sub_i32 s0, s0, s10
	s_sub_i32 s10, s0, s8
	s_cmp_ge_u32 s0, s8
	s_cselect_b32 s0, s10, s0
	s_sub_i32 s10, s0, s8
	s_cmp_ge_u32 s0, s8
	s_cselect_b32 s0, s10, s0
	s_xor_b32 s0, s0, s9
	s_sub_i32 s0, s0, s9
	s_add_i32 s1, s1, s0
	v_lshl_add_u32 v4, s1, 8, v1
	v_readlane_b32 s0, v254, 63
	v_ashrrev_i32_e32 v5, 31, v4
	v_readlane_b32 s1, v255, 0
	s_add_u32 s4, s4, s88
	s_addc_u32 s5, s5, s7
	v_lshl_add_u64 v[4:5], v[4:5], 4, s[0:1]
	global_load_dwordx4 v[112:115], v[4:5], off
	v_cmp_gt_i64_e32 vcc, s[4:5], v[252:253]
	s_and_b64 vcc, exec, vcc
	s_cbranch_vccnz .LBB0_290
	s_ashr_i32 s0, s4, 31
	s_lshr_b32 s0, s0, 29
	s_add_i32 s0, s4, s0
	s_ashr_i32 s1, s0, 3
	s_and_b32 s0, s0, -8
	s_sub_i32 s0, s4, s0
	s_cmp_lt_i32 s0, 0
	s_cselect_b32 s8, s17, 0xc0
	s_mul_i32 s0, s0, s8
	s_add_i32 s0, s0, s1
	s_mul_hi_i32 s1, s0, 0x2aaaaaab
	s_lshr_b32 s8, s1, 31
	s_ashr_i32 s1, s1, 4
	s_add_i32 s1, s1, s8
	s_mul_i32 s8, s1, 0x60
	s_lshl_b32 s1, s1, 3
	s_sub_i32 s0, s0, s8
	s_sub_i32 s8, 0x80, s1
	s_min_i32 s8, s8, 8
	s_abs_i32 s8, s8
	v_cvt_f32_u32_e32 v4, s8
	s_sub_i32 s10, 0, s8
	s_ashr_i32 s9, s0, 31
	s_abs_i32 s0, s0
	v_rcp_iflag_f32_e32 v4, v4
	s_nop 0
	v_mul_f32_e32 v4, 0x4f7ffffe, v4
	v_cvt_u32_f32_e32 v4, v4
	s_nop 0
	v_readfirstlane_b32 s11, v4
	s_mul_i32 s10, s10, s11
	s_mul_hi_u32 s10, s11, s10
	s_add_i32 s11, s11, s10
	s_mul_hi_u32 s10, s0, s11
	s_mul_i32 s10, s10, s8
	s_sub_i32 s0, s0, s10
	s_sub_i32 s10, s0, s8
	s_cmp_ge_u32 s0, s8
	s_cselect_b32 s0, s10, s0
	s_sub_i32 s10, s0, s8
	s_cmp_ge_u32 s0, s8
	s_cselect_b32 s0, s10, s0
	s_xor_b32 s0, s0, s9
	s_sub_i32 s0, s0, s9
	s_add_i32 s1, s1, s0
	v_lshl_add_u32 v4, s1, 8, v1
	v_readlane_b32 s0, v254, 63
	v_ashrrev_i32_e32 v5, 31, v4
	v_readlane_b32 s1, v255, 0
	s_add_u32 s4, s4, s88
	s_addc_u32 s5, s5, s7
	v_lshl_add_u64 v[4:5], v[4:5], 4, s[0:1]
	global_load_dwordx4 v[116:119], v[4:5], off
	v_cmp_gt_i64_e32 vcc, s[4:5], v[252:253]
	s_and_b64 vcc, exec, vcc
	s_cbranch_vccnz .LBB0_290
	s_ashr_i32 s0, s4, 31
	s_lshr_b32 s0, s0, 29
	s_add_i32 s0, s4, s0
	s_ashr_i32 s1, s0, 3
	s_and_b32 s0, s0, -8
	s_sub_i32 s0, s4, s0
	s_cmp_lt_i32 s0, 0
	s_cselect_b32 s8, s17, 0xc0
	s_mul_i32 s0, s0, s8
	s_add_i32 s0, s0, s1
	s_mul_hi_i32 s1, s0, 0x2aaaaaab
	s_lshr_b32 s8, s1, 31
	s_ashr_i32 s1, s1, 4
	s_add_i32 s1, s1, s8
	s_mul_i32 s8, s1, 0x60
	s_lshl_b32 s1, s1, 3
	s_sub_i32 s0, s0, s8
	s_sub_i32 s8, 0x80, s1
	s_min_i32 s8, s8, 8
	s_abs_i32 s8, s8
	v_cvt_f32_u32_e32 v4, s8
	s_sub_i32 s10, 0, s8
	s_ashr_i32 s9, s0, 31
	s_abs_i32 s0, s0
	v_rcp_iflag_f32_e32 v4, v4
	s_nop 0
	v_mul_f32_e32 v4, 0x4f7ffffe, v4
	v_cvt_u32_f32_e32 v4, v4
	s_nop 0
	v_readfirstlane_b32 s11, v4
	s_mul_i32 s10, s10, s11
	s_mul_hi_u32 s10, s11, s10
	s_add_i32 s11, s11, s10
	s_mul_hi_u32 s10, s0, s11
	s_mul_i32 s10, s10, s8
	s_sub_i32 s0, s0, s10
	s_sub_i32 s10, s0, s8
	s_cmp_ge_u32 s0, s8
	s_cselect_b32 s0, s10, s0
	s_sub_i32 s10, s0, s8
	s_cmp_ge_u32 s0, s8
	s_cselect_b32 s0, s10, s0
	s_xor_b32 s0, s0, s9
	s_sub_i32 s0, s0, s9
	s_add_i32 s1, s1, s0
	v_lshl_add_u32 v4, s1, 8, v1
	v_readlane_b32 s0, v254, 63
	v_ashrrev_i32_e32 v5, 31, v4
	v_readlane_b32 s1, v255, 0
	s_add_u32 s4, s4, s88
	s_addc_u32 s5, s5, s7
	v_lshl_add_u64 v[4:5], v[4:5], 4, s[0:1]
	global_load_dwordx4 v[120:123], v[4:5], off
	v_cmp_gt_i64_e32 vcc, s[4:5], v[252:253]
	s_and_b64 vcc, exec, vcc
	s_cbranch_vccnz .LBB0_290
	s_ashr_i32 s0, s4, 31
	s_lshr_b32 s0, s0, 29
	s_add_i32 s0, s4, s0
	s_ashr_i32 s1, s0, 3
	s_and_b32 s0, s0, -8
	s_sub_i32 s0, s4, s0
	s_cmp_lt_i32 s0, 0
	s_cselect_b32 s4, s17, 0xc0
	s_mul_i32 s0, s0, s4
	s_add_i32 s0, s0, s1
	s_mul_hi_i32 s1, s0, 0x2aaaaaab
	s_lshr_b32 s4, s1, 31
	s_ashr_i32 s1, s1, 4
	s_add_i32 s1, s1, s4
	s_lshl_b32 s4, s1, 3
	s_sub_i32 s5, 0x80, s4
	s_min_i32 s5, s5, 8
	s_abs_i32 s5, s5
	v_cvt_f32_u32_e32 v4, s5
	s_sub_i32 s7, 0, s5
	s_mulk_i32 s1, 0x60
	s_sub_i32 s0, s0, s1
	v_rcp_iflag_f32_e32 v4, v4
	s_ashr_i32 s1, s0, 31
	s_abs_i32 s0, s0
	v_mul_f32_e32 v4, 0x4f7ffffe, v4
	v_cvt_u32_f32_e32 v4, v4
	s_nop 0
	v_readfirstlane_b32 s8, v4
	s_mul_i32 s7, s7, s8
	s_mul_hi_u32 s7, s8, s7
	s_add_i32 s8, s8, s7
	s_mul_hi_u32 s7, s0, s8
	s_mul_i32 s7, s7, s5
	s_sub_i32 s0, s0, s7
	s_sub_i32 s7, s0, s5
	s_cmp_ge_u32 s0, s5
	s_cselect_b32 s0, s7, s0
	s_sub_i32 s7, s0, s5
	s_cmp_ge_u32 s0, s5
	s_cselect_b32 s0, s7, s0
	s_xor_b32 s0, s0, s1
	s_sub_i32 s0, s0, s1
	s_add_i32 s4, s4, s0
	v_lshl_add_u32 v4, s4, 8, v1
	v_readlane_b32 s0, v254, 63
	v_ashrrev_i32_e32 v5, 31, v4
	v_readlane_b32 s1, v255, 0
	s_nop 1
	v_lshl_add_u64 v[4:5], v[4:5], 4, s[0:1]
	global_load_dwordx4 v[124:127], v[4:5], off
; template <class Sched> __device__ __forceinline__ void stage_scales(PG8_LAS unsigned char* lds, const Sched& S, const float* rs, bool cols, int ldil, int tid) {
;     ...
;         for (int i = 0; i < 16 && S.next(i, u); ++i) { const f32x4 a = *(const f32x4*)(rs + 4 * (size_t)(cols ? u.pn * BM + tm : u.pm * BM + tid));
;             tab[i * 256 + tid] = __builtin_amdgcn_rsqf(((a[0] + a[1]) + (a[2] + a[3])) * (1.0f / 1024.0f) + eps); } }
;     __syncthreads();
.LBB0_290:
	s_waitcnt vmcnt(0)
	v_mov_b32_e32 v4, s6
	v_add_f32_e32 v8, v65, v64
	v_add_f32_e32 v9, v66, v67
	v_add_f32_e32 v8, v8, v9
	v_fmamk_f32 v8, v8, 0x3a800000, v4
	v_rsq_f32_e32 v8, v8
	s_nop 1
	ds_write_b32 v0, v8
	v_add_f32_e32 v8, v69, v68
	v_add_f32_e32 v9, v70, v71
	v_add_f32_e32 v8, v8, v9
	v_fmamk_f32 v8, v8, 0x3a800000, v4
	v_rsq_f32_e32 v8, v8
	s_nop 1
	ds_write_b32 v0, v8 offset:1024
	v_add_f32_e32 v8, v73, v72
	v_add_f32_e32 v9, v74, v75
	v_add_f32_e32 v8, v8, v9
	v_fmamk_f32 v8, v8, 0x3a800000, v4
	v_rsq_f32_e32 v8, v8
	s_nop 1
	ds_write_b32 v0, v8 offset:2048
	v_add_f32_e32 v8, v77, v76
	v_add_f32_e32 v9, v78, v79
	v_add_f32_e32 v8, v8, v9
	v_fmamk_f32 v8, v8, 0x3a800000, v4
	v_rsq_f32_e32 v8, v8
	s_nop 1
	ds_write_b32 v0, v8 offset:3072
	v_add_f32_e32 v8, v81, v80
	v_add_f32_e32 v9, v82, v83
	v_add_f32_e32 v8, v8, v9
	v_fmamk_f32 v8, v8, 0x3a800000, v4
	v_rsq_f32_e32 v8, v8
	s_nop 1
	ds_write_b32 v0, v8 offset:4096
	v_add_f32_e32 v8, v85, v84
	v_add_f32_e32 v9, v86, v87
	v_add_f32_e32 v8, v8, v9
	v_fmamk_f32 v8, v8, 0x3a800000, v4
	v_rsq_f32_e32 v8, v8
	s_nop 1
	ds_write_b32 v0, v8 offset:5120
	v_add_f32_e32 v8, v89, v88
	v_add_f32_e32 v9, v90, v91
	v_add_f32_e32 v8, v8, v9
	v_fmamk_f32 v8, v8, 0x3a800000, v4
	v_rsq_f32_e32 v8, v8
	s_nop 1
	ds_write_b32 v0, v8 offset:6144
	v_add_f32_e32 v8, v93, v92
	v_add_f32_e32 v9, v94, v95
	v_add_f32_e32 v8, v8, v9
	v_fmamk_f32 v8, v8, 0x3a800000, v4
	v_rsq_f32_e32 v8, v8
	s_nop 1
	ds_write_b32 v0, v8 offset:7168
	v_add_f32_e32 v8, v97, v96
	v_add_f32_e32 v9, v98, v99
	v_add_f32_e32 v8, v8, v9
	v_fmamk_f32 v8, v8, 0x3a800000, v4
	v_rsq_f32_e32 v8, v8
	s_nop 1
	ds_write_b32 v0, v8 offset:8192
	v_add_f32_e32 v8, v101, v100
	v_add_f32_e32 v9, v102, v103
	v_add_f32_e32 v8, v8, v9
	v_fmamk_f32 v8, v8, 0x3a800000, v4
	v_rsq_f32_e32 v8, v8
	s_nop 1
	ds_write_b32 v0, v8 offset:9216
	v_add_f32_e32 v8, v105, v104
	v_add_f32_e32 v9, v106, v107
	v_add_f32_e32 v8, v8, v9
	v_fmamk_f32 v8, v8, 0x3a800000, v4
	v_rsq_f32_e32 v8, v8
	s_nop 1
	ds_write_b32 v0, v8 offset:10240
	v_add_f32_e32 v8, v109, v108
	v_add_f32_e32 v9, v110, v111
	v_add_f32_e32 v8, v8, v9
	v_fmamk_f32 v8, v8, 0x3a800000, v4
	v_rsq_f32_e32 v8, v8
	s_nop 1
	ds_write_b32 v0, v8 offset:11264
	v_add_f32_e32 v8, v113, v112
	v_add_f32_e32 v9, v114, v115
	v_add_f32_e32 v8, v8, v9
	v_fmamk_f32 v8, v8, 0x3a800000, v4
	v_rsq_f32_e32 v8, v8
	s_nop 1
	ds_write_b32 v0, v8 offset:12288
	v_add_f32_e32 v8, v117, v116
	v_add_f32_e32 v9, v118, v119
	v_add_f32_e32 v8, v8, v9
	v_fmamk_f32 v8, v8, 0x3a800000, v4
	v_rsq_f32_e32 v8, v8
	s_nop 1
	ds_write_b32 v0, v8 offset:13312
	v_add_f32_e32 v8, v121, v120
	v_add_f32_e32 v9, v122, v123
	v_add_f32_e32 v8, v8, v9
	v_fmamk_f32 v8, v8, 0x3a800000, v4
	v_rsq_f32_e32 v8, v8
	s_nop 1
	ds_write_b32 v0, v8 offset:14336
	v_add_f32_e32 v8, v125, v124
	v_add_f32_e32 v9, v126, v127
	v_add_f32_e32 v8, v8, v9
	v_fmamk_f32 v8, v8, 0x3a800000, v4
	v_rsq_f32_e32 v8, v8
	s_nop 1
	ds_write_b32 v0, v8 offset:15360
	s_or_b64 exec, exec, s[2:3]
	s_cmpk_gt_i32 s90, 0x5ff
	v_readfirstlane_b32 s3, v1
	s_waitcnt vmcnt(0) lgkmcnt(0)
	s_barrier
	s_cbranch_scc1 .LBB0_308
; #define PG8_BAR __builtin_amdgcn_s_barrier()
;     __host__ __device__ bool next(int i, Unit& u) const {
;     ...
;         int wgid = (int)L; { const int q = nwg / NXCD, r = nwg % NXCD, xcd = wgid % NXCD, off = wgid / NXCD; wgid = (xcd < r ? xcd * (q + 1) : r * (q + 1) + (xcd - r) * q) + off; }
;         const int nig = WGM * nN, gid = wgid / nig, fm = gid * WGM, gsz = (nM - fm) < WGM ? (nM - fm) : WGM;
;         u.pm = fm + ((wgid % nig) % gsz); u.pn = (wgid % nig) / gsz; u.idx = i; return true;
; template <class Epi, class Sched, bool ALIGN_EPI = false, bool SP2 = false>
; __device__ __forceinline__ void gemm_phase(PG8_LAS unsigned char* lds, const Gemm g, const Sched& S, const Epi& E, const int tid) {
;     ...
;     for (int i = 0; i < 2; ++i) { int R, C; stage_rc(tid * 16 + i * 8192, R, C); const int Rb = Epi::PERM ? ((R & ~31) + perm32(R & 31)) : R;
;         voffA[i] = (unsigned)(R * K + C) * 2u; { const int ld = g.ldil, lper = 8 - ld, pm1 = (1 << lper) - 1; const int c0 = Rb, c1 = 128 + Rb; voffB[i] = (unsigned)((((c0 & pm1) << ld) + (c0 >> lper)) * K + C) * 2u; voffB1[i] = (unsigned)((((c1 & pm1) << ld) + (c1 >> lper)) * K + C) * 2u; } }
;     const size_t kstep = (size_t)(BK * 2);
;     const size_t hstep = (size_t)HALF * K * 2;
;     const size_t tstep = 2 * hstep;
;     const unsigned ldsw = (unsigned)wid * 1024u;
;     const int aoff = lds_byte(wr * 64 + fr, fq * 8), boff = lds_byte(wc * 32 + fr, fq * 8);
;     ...
;     Unit cur, nxt; int ui = 0;
;     if (!S.next(0, cur)) return;
;     f32x4 acc[2][2][4][2];
; #pragma unroll
;     for (int a = 0; a < 2; ++a)
; #pragma unroll
;         for (int b = 0; b < 2; ++b)
; #pragma unroll
;             for (int m = 0; m < 4; ++m)
; #pragma unroll
;                 for (int n = 0; n < 2; ++n) acc[a][b][m][n] = (f32x4){0.f, 0.f, 0.f, 0.f};
;     bf16x8 At[4][2], B0[2][2], B1[2][2];
;     const char* cA = (const char*)g.A + (size_t)cur.pm * tstep; const char* cB = (const char*)g.Bt + (size_t)cur.pn * tstep;
;     S.a_ready(cur);
;     if constexpr (SP2) {
;         PG8_STAGE(PG8_SB(0, 0), cB, voffB); PG8_STAGE(PG8_SB(0, 1), cB, voffB1); PG8_STAGE(PG8_SA(0, 0), cA, voffA); PG8_STAGE(PG8_SA(0, 1), cA + hstep, voffA);
;         if (wr == 1) PG8_BAR;
	v_lshlrev_b32_e32 v4, 4, v1
	v_add_u32_e32 v0, 0x2000, v4
	v_ashrrev_i32_e32 v5, 31, v0
	v_lshrrev_b32_e32 v5, 22, v5
	v_add_u32_e32 v5, v0, v5
	v_ashrrev_i32_e32 v16, 10, v5
	v_mul_i32_i24_e32 v5, 0x400, v16
	v_sub_u32_e32 v0, v0, v5
	v_lshrrev_b32_e32 v5, 4, v0
	v_bitop3_b32 v0, v5, v0, 32 bitop3:0x6c
	v_ashrrev_i32_e32 v5, 31, v0
	v_lshrrev_b32_e32 v5, 26, v5
	v_add_u32_e32 v5, v0, v5
	v_lshlrev_b32_e32 v6, 3, v16
	v_ashrrev_i32_e32 v17, 6, v5
	v_and_b32_e32 v6, -16, v6
	v_add_u32_e32 v6, v17, v6
	s_ashr_i32 s6, s3, 6
	v_lshrrev_b32_e32 v9, 2, v6
	s_ashr_i32 s7, s3, 8
	s_lshl_b32 s0, s6, 10
	v_and_b32_e32 v7, 0xffffffe0, v6
	v_and_b32_e32 v8, 3, v17
	v_and_b32_e32 v9, 4, v9
	s_add_u32 s1, s96, 0x1a00000
	v_or3_b32 v7, v7, v8, v9
	v_lshlrev_b32_e32 v8, 1, v6
	s_addc_u32 s33, s97, 0
	s_mul_i32 s4, s24, 0x600000
	v_and_b32_e32 v8, 24, v8
	s_mul_hi_u32 s2, s24, 0x600000
	s_add_u32 s4, s96, s4
	v_or_b32_e32 v9, v7, v8
	s_addc_u32 s2, s97, s2
	v_add_u32_e32 v9, 0x80, v9
	v_and_b32_e32 v5, 0xc0, v5
	s_add_u32 s38, s4, 0x200000
	v_lshrrev_b32_e32 v10, 8, v9
	v_sub_u32_e32 v0, v0, v5
	s_addc_u32 s39, s2, 0
	v_add_u32_sdwa v9, v9, v10 dst_sel:DWORD dst_unused:UNUSED_PAD src0_sel:BYTE_0 src1_sel:DWORD
	v_lshlrev_b32_e32 v10, 5, v16
	v_ashrrev_i16_sdwa v0, v235, sext(v0) dst_sel:DWORD dst_unused:UNUSED_PAD src0_sel:DWORD src1_sel:BYTE_0
	s_ashr_i32 s40, s90, 31
	v_and_b32_e32 v10, 32, v10
	v_bfe_i32 v18, v0, 0, 16
	v_bitop3_b32 v7, v7, s70, v8 bitop3:0xc8
	v_lshrrev_b32_e32 v8, 8, v6
	s_lshr_b32 s2, s40, 29
	v_add_lshl_u32 v5, v10, v18, 1
	v_add_u32_e32 v7, v7, v8
	s_add_i32 s2, s90, s2
	v_lshl_add_u32 v0, v9, 11, v5
	v_lshl_add_u32 v132, v7, 11, v5
	v_lshl_add_u32 v134, v6, 11, v5
	v_bfe_i32 v5, v1, 27, 1
	s_ashr_i32 s4, s2, 3
	s_and_b32 s2, s2, -8
	v_lshrrev_b32_e32 v5, 22, v5
	s_sub_i32 s2, s90, s2
	v_add_u32_e32 v5, v4, v5
	s_cmp_lt_i32 s2, 0
	v_and_b32_e32 v5, 0xfffffc00, v5
	s_cselect_b32 s5, s17, 0xc0
	v_sub_u32_e32 v4, v4, v5
	s_mul_i32 s2, s2, s5
	v_lshrrev_b32_e32 v5, 4, v4
	v_ashrrev_i32_e32 v6, 31, v1
	s_add_i32 s2, s2, s4
	v_bitop3_b32 v4, v5, v4, 32 bitop3:0x6c
	v_lshrrev_b32_e32 v6, 26, v6
	s_mul_hi_i32 s4, s2, 0x2aaaaaab
	v_ashrrev_i32_e32 v5, 31, v4
	v_add_u32_e32 v1, v1, v6
	s_lshr_b32 s5, s4, 31
	s_ashr_i32 s4, s4, 4
	v_lshrrev_b32_e32 v5, 26, v5
	v_ashrrev_i32_e32 v20, 6, v1
	s_add_i32 s4, s4, s5
	v_add_u32_e32 v5, v4, v5
	v_lshlrev_b32_e32 v1, 3, v20
	s_lshl_b32 s5, s4, 3
	s_mulk_i32 s4, 0x60
	v_ashrrev_i32_e32 v19, 6, v5
	v_and_b32_e32 v1, -16, v1
	s_sub_i32 s4, s2, s4
	v_add_u32_e32 v1, v19, v1
	s_bfe_i32 s2, s4, 0x80000
	v_lshrrev_b32_e32 v8, 2, v1
	s_bfe_u32 s2, s2, 0x3000c
	v_and_b32_e32 v6, 0xffffffe0, v1
	v_and_b32_e32 v7, 3, v19
	v_and_b32_e32 v8, 4, v8
	s_add_i32 s8, s4, s2
	v_or3_b32 v6, v6, v7, v8
	v_lshlrev_b32_e32 v7, 1, v1
	s_bfe_i32 s2, s8, 0x80000
	s_and_b32 s8, s8, 0xf8
	v_and_b32_e32 v7, 24, v7
	s_sub_i32 s4, s4, s8
	v_or_b32_e32 v8, v6, v7
	s_sext_i32_i16 s2, s2
	s_sext_i32_i8 s4, s4
	v_add_u32_e32 v8, 0x80, v8
	v_and_b32_e32 v5, 0xc0, v5
	s_lshr_b32 s2, s2, 3
	s_add_i32 s44, s5, s4
	v_lshrrev_b32_e32 v9, 8, v8
	v_sub_u32_e32 v4, v4, v5
	s_ashr_i32 s45, s44, 31
	s_bfe_i64 s[8:9], s[2:3], 0x100000
	v_add_u32_sdwa v8, v8, v9 dst_sel:DWORD dst_unused:UNUSED_PAD src0_sel:BYTE_0 src1_sel:DWORD
	v_lshlrev_b32_e32 v9, 5, v20
	v_ashrrev_i16_sdwa v4, v235, sext(v4) dst_sel:DWORD dst_unused:UNUSED_PAD src0_sel:DWORD src1_sel:BYTE_0
	s_lshl_b64 s[4:5], s[44:45], 19
	s_lshl_b64 s[8:9], s[8:9], 19
	v_and_b32_e32 v9, 32, v9
	v_bfe_i32 v21, v4, 0, 16
	v_bitop3_b32 v5, v6, s70, v7 bitop3:0xc8
	v_lshrrev_b32_e32 v6, 8, v1
	s_add_u32 s52, s38, s8
	v_add_lshl_u32 v4, v9, v21, 1
	v_add_u32_e32 v5, v5, v6
	s_addc_u32 s53, s39, s9
	s_add_i32 s41, s0, 0
	v_lshl_add_u32 v138, v5, 11, v4
	s_add_i32 m0, s41, 0x10000
	v_lshl_add_u32 v136, v8, 11, v4
	global_load_lds_dwordx4 v138, s[52:53]
	s_add_i32 m0, s41, 0x12000
	v_lshl_add_u32 v140, v1, 11, v4
	global_load_lds_dwordx4 v132, s[52:53]
	s_add_i32 m0, s41, 0x14000
	v_mov_b32_e32 v139, v3
	global_load_lds_dwordx4 v136, s[52:53]
	s_add_i32 m0, s41, 0x16000
	s_add_u32 s46, s1, s4
	s_addc_u32 s47, s33, s5
	s_add_i32 s42, s41, 0x2000
	global_load_lds_dwordx4 v0, s[52:53]
	s_mov_b32 m0, s41
	s_add_u32 s4, s46, 0x40000
	global_load_lds_dwordx4 v140, s[46:47]
	s_mov_b32 m0, s42
	s_addc_u32 s5, s47, 0
	s_add_i32 s43, s41, 0x4000
	global_load_lds_dwordx4 v134, s[46:47]
	s_mov_b32 m0, s43
	s_add_i32 s48, s41, 0x6000
	global_load_lds_dwordx4 v140, s[4:5]
	s_mov_b32 m0, s48
	v_mov_b32_e32 v133, v3
	global_load_lds_dwordx4 v134, s[4:5]
	v_mov_b32_e32 v137, v3
	v_mov_b32_e32 v1, v3
	v_mov_b32_e32 v141, v3
	v_mov_b32_e32 v135, v3
	s_cmp_eq_u32 s7, 1
	v_lshl_add_u64 v[10:11], s[52:53], 0, v[138:139]
	v_lshl_add_u64 v[8:9], s[52:53], 0, v[132:133]
	v_lshl_add_u64 v[6:7], s[52:53], 0, v[136:137]
	v_lshl_add_u64 v[4:5], s[52:53], 0, v[0:1]
	v_lshl_add_u64 v[12:13], s[46:47], 0, v[140:141]
	s_cselect_b64 s[4:5], -1, 0
	s_cmp_lg_u32 s7, 1
	v_lshl_add_u64 v[14:15], s[46:47], 0, v[134:135]
	s_cbranch_scc1 .LBB0_293
	s_barrier
